# attention flash loops: wave priority raised during the softmax (VALU) stage instead of the MFMA stage
# baseline (speedup 1.0000x reference)
; #define LAS __attribute__((address_space(3)))
; #define VM_WAIT() asm volatile("s_waitcnt vmcnt(0)" ::: "memory")
; #define SBAR() __builtin_amdgcn_sched_barrier(0)
; template <int OFF> __device__ __forceinline__ s16x4 tr_read(int vb) { s16x4 r; asm volatile("ds_read_b64_tr_b16 %0, %1 offset:%2" : "=&v"(r) : "v"(vb), "i"(OFF) : "memory"); return r; }
; #define BAR() do { asm volatile("" ::: "memory"); __builtin_amdgcn_s_barrier(); asm volatile("" ::: "memory"); } while (0)
; __device__ __forceinline__ void qkt(f32x16& p0, f32x16& p1, const LAS char* Ks, const bf16x8 (&qr)[8], int r32, int hi) {
;     p0 = f32x16{}; p1 = f32x16{};
; #pragma unroll
;     for (int d0 = 0; d0 < 8; ++d0) { const int cb = (d0 * 16 + hi * 8) * 2;
;         const bf16x8 b0 = *(const LAS bf16x8*)(Ks + KSWZ(r32, cb));
;         const bf16x8 b1 = *(const LAS bf16x8*)(Ks + KSWZ(32 + r32, cb));
;         p0 = __builtin_amdgcn_mfma_f32_32x32x16_bf16(b0, qr[d0], p0, 0, 0, 0);
;         p1 = __builtin_amdgcn_mfma_f32_32x32x16_bf16(b1, qr[d0], p1, 0, 0, 0);
;         if (d0 == 3) SBAR(); }
; }
; template <int D0> __device__ __forceinline__ void pv_one(f32x16& od, int vb, bf16x8 pa0, bf16x8 pa1, bf16x8 pa2, bf16x8 pa3) {
;     const s16x4 l0 = tr_read<v_rd_off(D0, 0, 0)>(vb), h0 = tr_read<v_rd_off(D0, 0, 1)>(vb), l1 = tr_read<v_rd_off(D0, 1, 0)>(vb), h1 = tr_read<v_rd_off(D0, 1, 1)>(vb);
;     const s16x4 l2 = tr_read<v_rd_off(D0, 2, 0)>(vb), h2 = tr_read<v_rd_off(D0, 2, 1)>(vb), l3 = tr_read<v_rd_off(D0, 3, 0)>(vb), h3 = tr_read<v_rd_off(D0, 3, 1)>(vb);
;     asm volatile("s_waitcnt lgkmcnt(0)" ::: "memory"); SBAR();
;     ...
;     od = __builtin_amdgcn_mfma_f32_32x32x16_bf16(pa0, PK(l0, h0), od, 0, 0, 0);
;     od = __builtin_amdgcn_mfma_f32_32x32x16_bf16(pa1, PK(l1, h1), od, 0, 0, 0);
;     od = __builtin_amdgcn_mfma_f32_32x32x16_bf16(pa2, PK(l2, h2), od, 0, 0, 0);
;     od = __builtin_amdgcn_mfma_f32_32x32x16_bf16(pa3, PK(l3, h3), od, 0, 0, 0);
;     ...
; }
; template <int MODE> ...
;     ...
;         if (half == 0 && i + 1 >= 3 && i + 1 < n) DMA(i + 1, nslot);
;         if (i > 0) PV(pslot);
;         f32x16 p0, p1;
;         qkt(p0, p1, K_lds + buf * SHM, qr, r32, hi);
;         if (half == 1) VM_WAIT();
;         BAR();
;         if (half == 1 && i + 2 >= 3 && i + 2 < n) DMA(i + 2, pslot);
.LBB0_599:
	s_setprio 0
	s_lshl_b32 s29, s17, 14
	s_add_i32 s34, s29, 0xffffc000
	s_cmp_lg_u32 s17, 0
	s_cselect_b32 s17, s34, 0x8000
	v_add_u32_e32 v144, s17, v165
	ds_read_b64_tr_b16 v[84:85], v144 offset:0
	ds_read_b64_tr_b16 v[86:87], v144 offset:0x800
	ds_read_b64_tr_b16 v[88:89], v144 offset:0x1000
	ds_read_b64_tr_b16 v[90:91], v144 offset:0x1800
	ds_read_b64_tr_b16 v[92:93], v144 offset:0x2000
	ds_read_b64_tr_b16 v[94:95], v144 offset:0x2800
	ds_read_b64_tr_b16 v[96:97], v144 offset:0x3000
	ds_read_b64_tr_b16 v[98:99], v144 offset:0x3800
	s_waitcnt lgkmcnt(0)
	s_nop 0
	v_mfma_f32_32x32x16_bf16 v[20:35], v[72:75], v[84:87], v[20:35]
	ds_read_b64_tr_b16 v[84:85], v144 offset:0x200
	ds_read_b64_tr_b16 v[86:87], v144 offset:0xa00
	v_add_u32_e32 v246, s29, v148
	v_add_u32_e32 v247, v246, v149
	ds_read_b128 v[212:215], v247 offset:49152
	v_mfma_f32_32x32x16_bf16 v[20:35], v[76:79], v[88:91], v[20:35]
	ds_read_b64_tr_b16 v[88:89], v144 offset:0x1200
	ds_read_b64_tr_b16 v[90:91], v144 offset:0x1a00
	ds_read_b128 v[216:219], v247 offset:57344
	v_mfma_f32_32x32x16_bf16 v[20:35], v[80:83], v[92:95], v[20:35]
	ds_read_b64_tr_b16 v[92:93], v144 offset:0x2200
	ds_read_b64_tr_b16 v[94:95], v144 offset:0x2a00
	v_add_u32_e32 v247, v246, v150
	ds_read_b128 v[220:223], v247 offset:49152
	v_mfma_f32_32x32x16_bf16 v[20:35], v[68:71], v[96:99], v[20:35]
	ds_read_b64_tr_b16 v[96:97], v144 offset:0x3200
	ds_read_b64_tr_b16 v[98:99], v144 offset:0x3a00
	ds_read_b128 v[224:227], v247 offset:57344
	s_waitcnt lgkmcnt(0)
	v_mfma_f32_32x32x16_bf16 v[36:51], v[72:75], v[84:87], v[36:51]
	ds_read_b64_tr_b16 v[84:85], v144 offset:0x400
	ds_read_b64_tr_b16 v[86:87], v144 offset:0xc00
	v_add_u32_e32 v247, v246, v151
	ds_read_b128 v[228:231], v247 offset:49152
	v_mfma_f32_32x32x16_bf16 v[36:51], v[76:79], v[88:91], v[36:51]
	ds_read_b64_tr_b16 v[88:89], v144 offset:0x1400
	ds_read_b64_tr_b16 v[90:91], v144 offset:0x1c00
	ds_read_b128 v[232:235], v247 offset:57344
	v_mfma_f32_32x32x16_bf16 v[36:51], v[80:83], v[92:95], v[36:51]
	ds_read_b64_tr_b16 v[92:93], v144 offset:0x2400
	ds_read_b64_tr_b16 v[94:95], v144 offset:0x2c00
	v_add_u32_e32 v247, v246, v167
	ds_read_b128 v[236:239], v247 offset:49152
	v_mfma_f32_32x32x16_bf16 v[36:51], v[68:71], v[96:99], v[36:51]
	ds_read_b64_tr_b16 v[96:97], v144 offset:0x3400
	ds_read_b64_tr_b16 v[98:99], v144 offset:0x3c00
	ds_read_b128 v[240:243], v247 offset:57344
	s_waitcnt lgkmcnt(0)
	v_mfma_f32_32x32x16_bf16 v[52:67], v[72:75], v[84:87], v[52:67]
	ds_read_b64_tr_b16 v[84:85], v144 offset:0x600
	ds_read_b64_tr_b16 v[86:87], v144 offset:0xe00
	v_mfma_f32_32x32x16_bf16 v[52:67], v[76:79], v[88:91], v[52:67]
	ds_read_b64_tr_b16 v[88:89], v144 offset:0x1600
	ds_read_b64_tr_b16 v[90:91], v144 offset:0x1e00
	v_mfma_f32_32x32x16_bf16 v[52:67], v[80:83], v[92:95], v[52:67]
	ds_read_b64_tr_b16 v[92:93], v144 offset:0x2600
	ds_read_b64_tr_b16 v[94:95], v144 offset:0x2e00
	v_mfma_f32_32x32x16_bf16 v[52:67], v[68:71], v[96:99], v[52:67]
	ds_read_b64_tr_b16 v[96:97], v144 offset:0x3600
	ds_read_b64_tr_b16 v[98:99], v144 offset:0x3e00
	s_waitcnt lgkmcnt(0)
	v_mfma_f32_32x32x16_bf16 v[4:19], v[72:75], v[84:87], v[4:19]
	v_mfma_f32_32x32x16_bf16 v[4:19], v[76:79], v[88:91], v[4:19]
	v_mfma_f32_32x32x16_bf16 v[4:19], v[80:83], v[92:95], v[4:19]
	v_mfma_f32_32x32x16_bf16 v[4:19], v[68:71], v[96:99], v[4:19]
	s_and_b64 vcc, exec, s[12:13]
	v_mfma_f32_32x32x16_bf16 v[68:83], v[212:215], v[124:127], 0
	v_add_u32_e32 v247, v246, v169
	ds_read_b128 v[212:215], v247 offset:49152
	v_mfma_f32_32x32x16_bf16 v[84:99], v[216:219], v[124:127], 0
	ds_read_b128 v[216:219], v247 offset:57344
	v_mfma_f32_32x32x16_bf16 v[68:83], v[220:223], v[100:103], v[68:83]
	v_add_u32_e32 v247, v246, v176
	ds_read_b128 v[220:223], v247 offset:49152
	v_mfma_f32_32x32x16_bf16 v[84:99], v[224:227], v[100:103], v[84:99]
	ds_read_b128 v[224:227], v247 offset:57344
	v_mfma_f32_32x32x16_bf16 v[68:83], v[228:231], v[104:107], v[68:83]
	v_add_u32_e32 v247, v246, v177
	ds_read_b128 v[228:231], v247 offset:49152
	v_mfma_f32_32x32x16_bf16 v[84:99], v[232:235], v[104:107], v[84:99]
	ds_read_b128 v[232:235], v247 offset:57344
	v_mfma_f32_32x32x16_bf16 v[68:83], v[236:239], v[108:111], v[68:83]
	v_add_u32_e32 v247, v246, v178
	ds_read_b128 v[236:239], v247 offset:49152
	v_mfma_f32_32x32x16_bf16 v[84:99], v[240:243], v[108:111], v[84:99]
	ds_read_b128 v[240:243], v247 offset:57344
	s_waitcnt lgkmcnt(7)
	v_mfma_f32_32x32x16_bf16 v[68:83], v[212:215], v[112:115], v[68:83]
	s_waitcnt lgkmcnt(6)
	v_mfma_f32_32x32x16_bf16 v[84:99], v[216:219], v[112:115], v[84:99]
	s_waitcnt lgkmcnt(5)
	v_mfma_f32_32x32x16_bf16 v[68:83], v[220:223], v[116:119], v[68:83]
	s_waitcnt lgkmcnt(4)
	v_mfma_f32_32x32x16_bf16 v[84:99], v[224:227], v[116:119], v[84:99]
	s_waitcnt lgkmcnt(3)
	v_mfma_f32_32x32x16_bf16 v[68:83], v[228:231], v[120:123], v[68:83]
	s_waitcnt lgkmcnt(2)
	v_mfma_f32_32x32x16_bf16 v[84:99], v[232:235], v[120:123], v[84:99]
	s_waitcnt lgkmcnt(1)
	v_mfma_f32_32x32x16_bf16 v[68:83], v[236:239], v[128:131], v[68:83]
	s_waitcnt lgkmcnt(0)
	v_mfma_f32_32x32x16_bf16 v[84:99], v[240:243], v[128:131], v[84:99]
	s_cbranch_vccnz .LBB0_601
	s_waitcnt vmcnt(0)
.LBB0_601:
	s_setprio 1
	s_barrier
	s_and_b64 vcc, exec, s[12:13]
	s_cbranch_vccnz .LBB0_604
	s_add_i32 s29, s28, 2
	s_cmp_ge_i32 s29, s18
	s_cbranch_scc1 .LBB0_604
	v_mov_b32_e32 v144, s27
	ds_read_b32 v144, v144
	s_waitcnt lgkmcnt(0)
	v_readfirstlane_b32 s34, v144
	s_ashr_i32 s35, s34, 31
	s_lshl_b64 s[34:35], s[34:35], 14
	s_add_u32 s36, s14, s34
	s_addc_u32 s37, s15, s35
	s_add_i32 s17, s21, s17
	s_add_i32 m0, s17, 0xc000
	v_lshl_add_u64 v[144:145], v[136:137], 1, s[36:37]
	global_load_lds_dwordx4 v[144:145], off
	s_add_i32 m0, s17, 0xc400
	s_add_u32 s34, s19, s34
	v_lshl_add_u64 v[144:145], v[140:141], 1, s[36:37]
	s_addc_u32 s35, s20, s35
	global_load_lds_dwordx4 v[144:145], off
	v_lshl_add_u64 v[144:145], v[138:139], 1, s[34:35]
	s_mov_b32 m0, s17
	s_movk_i32 s37, 0x1af
	global_load_lds_dwordx4 v[144:145], off
	v_lshl_add_u64 v[144:145], v[142:143], 1, s[34:35]
	s_add_i32 m0, s17, 0x400
	s_movk_i32 s36, 0x7f
	global_load_lds_dwordx4 v[144:145], off

; #define LAS __attribute__((address_space(3)))
; #define VM_WAIT() asm volatile("s_waitcnt vmcnt(0)" ::: "memory")
; #define SBAR() __builtin_amdgcn_sched_barrier(0)
; template <int OFF> __device__ __forceinline__ s16x4 tr_read(int vb) { s16x4 r; asm volatile("ds_read_b64_tr_b16 %0, %1 offset:%2" : "=&v"(r) : "v"(vb), "i"(OFF) : "memory"); return r; }
; #define BAR() do { asm volatile("" ::: "memory"); __builtin_amdgcn_s_barrier(); asm volatile("" ::: "memory"); } while (0)
; __device__ __forceinline__ void qkt(f32x16& p0, f32x16& p1, const LAS char* Ks, const bf16x8 (&qr)[8], int r32, int hi) {
;     p0 = f32x16{}; p1 = f32x16{};
; #pragma unroll
;     for (int d0 = 0; d0 < 8; ++d0) { const int cb = (d0 * 16 + hi * 8) * 2;
;         const bf16x8 b0 = *(const LAS bf16x8*)(Ks + KSWZ(r32, cb));
;         const bf16x8 b1 = *(const LAS bf16x8*)(Ks + KSWZ(32 + r32, cb));
;         p0 = __builtin_amdgcn_mfma_f32_32x32x16_bf16(b0, qr[d0], p0, 0, 0, 0);
;         p1 = __builtin_amdgcn_mfma_f32_32x32x16_bf16(b1, qr[d0], p1, 0, 0, 0);
;         if (d0 == 3) SBAR(); }
; }
; template <int D0> __device__ __forceinline__ void pv_one(f32x16& od, int vb, bf16x8 pa0, bf16x8 pa1, bf16x8 pa2, bf16x8 pa3) {
;     const s16x4 l0 = tr_read<v_rd_off(D0, 0, 0)>(vb), h0 = tr_read<v_rd_off(D0, 0, 1)>(vb), l1 = tr_read<v_rd_off(D0, 1, 0)>(vb), h1 = tr_read<v_rd_off(D0, 1, 1)>(vb);
;     const s16x4 l2 = tr_read<v_rd_off(D0, 2, 0)>(vb), h2 = tr_read<v_rd_off(D0, 2, 1)>(vb), l3 = tr_read<v_rd_off(D0, 3, 0)>(vb), h3 = tr_read<v_rd_off(D0, 3, 1)>(vb);
;     asm volatile("s_waitcnt lgkmcnt(0)" ::: "memory"); SBAR();
;     ...
;     od = __builtin_amdgcn_mfma_f32_32x32x16_bf16(pa0, PK(l0, h0), od, 0, 0, 0);
;     od = __builtin_amdgcn_mfma_f32_32x32x16_bf16(pa1, PK(l1, h1), od, 0, 0, 0);
;     od = __builtin_amdgcn_mfma_f32_32x32x16_bf16(pa2, PK(l2, h2), od, 0, 0, 0);
;     od = __builtin_amdgcn_mfma_f32_32x32x16_bf16(pa3, PK(l3, h3), od, 0, 0, 0);
;     ...
; }
; template <int MODE> ...
;     ...
;         if (half == 0 && i + 1 >= 3 && i + 1 < n) DMA(i + 1, nslot);
;         if (i > 0) PV(pslot);
;         f32x16 p0, p1;
;         qkt(p0, p1, K_lds + buf * SHM, qr, r32, hi);
;         if (half == 1) VM_WAIT();
;         BAR();
;         if (half == 1 && i + 2 >= 3 && i + 2 < n) DMA(i + 2, pslot);
.LBB0_775:
	s_setprio 0
	s_lshl_b32 s18, s13, 14
	s_add_i32 s19, s18, 0xffffc000
	s_cmp_lg_u32 s13, 0
	s_cselect_b32 s13, s19, 0x8000
	v_add_u32_e32 v188, s13, v165
	ds_read_b64_tr_b16 v[84:85], v188 offset:0
	ds_read_b64_tr_b16 v[86:87], v188 offset:0x800
	ds_read_b64_tr_b16 v[88:89], v188 offset:0x1000
	ds_read_b64_tr_b16 v[90:91], v188 offset:0x1800
	ds_read_b64_tr_b16 v[92:93], v188 offset:0x2000
	ds_read_b64_tr_b16 v[94:95], v188 offset:0x2800
	ds_read_b64_tr_b16 v[96:97], v188 offset:0x3000
	ds_read_b64_tr_b16 v[98:99], v188 offset:0x3800
	s_waitcnt lgkmcnt(0)
	s_nop 0
	v_mfma_f32_32x32x16_bf16 v[20:35], v[72:75], v[84:87], v[20:35]
	ds_read_b64_tr_b16 v[84:85], v188 offset:0x200
	ds_read_b64_tr_b16 v[86:87], v188 offset:0xa00
	v_add_u32_e32 v246, s18, v173
	v_add_u32_e32 v247, v246, v174
	ds_read_b128 v[212:215], v247 offset:49152
	v_mfma_f32_32x32x16_bf16 v[20:35], v[76:79], v[88:91], v[20:35]
	ds_read_b64_tr_b16 v[88:89], v188 offset:0x1200
	ds_read_b64_tr_b16 v[90:91], v188 offset:0x1a00
	ds_read_b128 v[216:219], v247 offset:57344
	v_mfma_f32_32x32x16_bf16 v[20:35], v[80:83], v[92:95], v[20:35]
	ds_read_b64_tr_b16 v[92:93], v188 offset:0x2200
	ds_read_b64_tr_b16 v[94:95], v188 offset:0x2a00
	v_add_u32_e32 v247, v246, v175
	ds_read_b128 v[220:223], v247 offset:49152
	v_mfma_f32_32x32x16_bf16 v[20:35], v[68:71], v[96:99], v[20:35]
	ds_read_b64_tr_b16 v[96:97], v188 offset:0x3200
	ds_read_b64_tr_b16 v[98:99], v188 offset:0x3a00
	ds_read_b128 v[224:227], v247 offset:57344
	s_waitcnt lgkmcnt(0)
	v_mfma_f32_32x32x16_bf16 v[36:51], v[72:75], v[84:87], v[36:51]
	ds_read_b64_tr_b16 v[84:85], v188 offset:0x400
	ds_read_b64_tr_b16 v[86:87], v188 offset:0xc00
	v_add_u32_e32 v247, v246, v176
	ds_read_b128 v[228:231], v247 offset:49152
	v_mfma_f32_32x32x16_bf16 v[36:51], v[76:79], v[88:91], v[36:51]
	ds_read_b64_tr_b16 v[88:89], v188 offset:0x1400
	ds_read_b64_tr_b16 v[90:91], v188 offset:0x1c00
	ds_read_b128 v[232:235], v247 offset:57344
	v_mfma_f32_32x32x16_bf16 v[36:51], v[80:83], v[92:95], v[36:51]
	ds_read_b64_tr_b16 v[92:93], v188 offset:0x2400
	ds_read_b64_tr_b16 v[94:95], v188 offset:0x2c00
	v_add_u32_e32 v247, v246, v177
	ds_read_b128 v[236:239], v247 offset:49152
	v_mfma_f32_32x32x16_bf16 v[36:51], v[68:71], v[96:99], v[36:51]
	ds_read_b64_tr_b16 v[96:97], v188 offset:0x3400
	ds_read_b64_tr_b16 v[98:99], v188 offset:0x3c00
	ds_read_b128 v[240:243], v247 offset:57344
	s_waitcnt lgkmcnt(0)
	v_mfma_f32_32x32x16_bf16 v[52:67], v[72:75], v[84:87], v[52:67]
	ds_read_b64_tr_b16 v[84:85], v188 offset:0x600
	ds_read_b64_tr_b16 v[86:87], v188 offset:0xe00
	v_mfma_f32_32x32x16_bf16 v[52:67], v[76:79], v[88:91], v[52:67]
	ds_read_b64_tr_b16 v[88:89], v188 offset:0x1600
	ds_read_b64_tr_b16 v[90:91], v188 offset:0x1e00
	v_mfma_f32_32x32x16_bf16 v[52:67], v[80:83], v[92:95], v[52:67]
	ds_read_b64_tr_b16 v[92:93], v188 offset:0x2600
	ds_read_b64_tr_b16 v[94:95], v188 offset:0x2e00
	v_mfma_f32_32x32x16_bf16 v[52:67], v[68:71], v[96:99], v[52:67]
	ds_read_b64_tr_b16 v[96:97], v188 offset:0x3600
	ds_read_b64_tr_b16 v[98:99], v188 offset:0x3e00
	s_waitcnt lgkmcnt(0)
	v_mfma_f32_32x32x16_bf16 v[4:19], v[72:75], v[84:87], v[4:19]
	v_mfma_f32_32x32x16_bf16 v[4:19], v[76:79], v[88:91], v[4:19]
	v_mfma_f32_32x32x16_bf16 v[4:19], v[80:83], v[92:95], v[4:19]
	v_mfma_f32_32x32x16_bf16 v[4:19], v[68:71], v[96:99], v[4:19]
	s_and_b64 vcc, exec, s[10:11]
	v_mfma_f32_32x32x16_bf16 v[68:83], v[212:215], v[124:127], 0
	v_add_u32_e32 v247, v246, v178
	ds_read_b128 v[212:215], v247 offset:49152
	v_mfma_f32_32x32x16_bf16 v[84:99], v[216:219], v[124:127], 0
	ds_read_b128 v[216:219], v247 offset:57344
	v_mfma_f32_32x32x16_bf16 v[68:83], v[220:223], v[100:103], v[68:83]
	v_add_u32_e32 v247, v246, v179
	ds_read_b128 v[220:223], v247 offset:49152
	v_mfma_f32_32x32x16_bf16 v[84:99], v[224:227], v[100:103], v[84:99]
	ds_read_b128 v[224:227], v247 offset:57344
	v_mfma_f32_32x32x16_bf16 v[68:83], v[228:231], v[104:107], v[68:83]
	v_add_u32_e32 v247, v246, v180
	ds_read_b128 v[228:231], v247 offset:49152
	v_mfma_f32_32x32x16_bf16 v[84:99], v[232:235], v[104:107], v[84:99]
	ds_read_b128 v[232:235], v247 offset:57344
	v_mfma_f32_32x32x16_bf16 v[68:83], v[236:239], v[108:111], v[68:83]
	v_add_u32_e32 v247, v246, v181
	ds_read_b128 v[236:239], v247 offset:49152
	v_mfma_f32_32x32x16_bf16 v[84:99], v[240:243], v[108:111], v[84:99]
	ds_read_b128 v[240:243], v247 offset:57344
	s_waitcnt lgkmcnt(7)
	v_mfma_f32_32x32x16_bf16 v[68:83], v[212:215], v[112:115], v[68:83]
	s_waitcnt lgkmcnt(6)
	v_mfma_f32_32x32x16_bf16 v[84:99], v[216:219], v[112:115], v[84:99]
	s_waitcnt lgkmcnt(5)
	v_mfma_f32_32x32x16_bf16 v[68:83], v[220:223], v[116:119], v[68:83]
	s_waitcnt lgkmcnt(4)
	v_mfma_f32_32x32x16_bf16 v[84:99], v[224:227], v[116:119], v[84:99]
	s_waitcnt lgkmcnt(3)
	v_mfma_f32_32x32x16_bf16 v[68:83], v[228:231], v[120:123], v[68:83]
	s_waitcnt lgkmcnt(2)
	v_mfma_f32_32x32x16_bf16 v[84:99], v[232:235], v[120:123], v[84:99]
	s_waitcnt lgkmcnt(1)
	v_mfma_f32_32x32x16_bf16 v[68:83], v[236:239], v[128:131], v[68:83]
	s_waitcnt lgkmcnt(0)
	v_mfma_f32_32x32x16_bf16 v[84:99], v[240:243], v[128:131], v[84:99]
	s_cbranch_vccnz .LBB0_777
	s_waitcnt vmcnt(0)
.LBB0_777:
	s_setprio 1
	s_barrier
	s_and_b64 vcc, exec, s[10:11]
	s_cbranch_vccnz .LBB0_780
	s_add_i32 s18, s17, 2
	s_cmp_ge_i32 s18, s6
	s_cbranch_scc1 .LBB0_780
	v_mov_b32_e32 v188, s7
	ds_read_b32 v188, v188
	s_mov_b64 s[20:21], 0x800
	s_waitcnt lgkmcnt(0)
	v_readfirstlane_b32 s18, v188
	s_mul_hi_i32 s19, s18, 0x1e8000
	s_mul_i32 s18, s18, 0x1e8000
	s_add_u32 s18, s14, s18
	s_addc_u32 s19, s15, s19
	s_add_i32 s13, s90, s13
	v_lshl_add_u64 v[188:189], v[152:153], 1, s[18:19]
	s_add_i32 m0, s13, 0xc000
	v_lshl_add_u64 v[188:189], v[188:189], 0, s[20:21]
	global_load_lds_dwordx4 v[188:189], off
	v_lshl_add_u64 v[188:189], v[156:157], 1, s[18:19]
	v_lshl_add_u64 v[188:189], v[188:189], 0, s[20:21]
	s_add_i32 m0, s13, 0xc400
	s_mov_b64 s[20:21], 0xc00
	global_load_lds_dwordx4 v[188:189], off
	v_lshl_add_u64 v[188:189], v[154:155], 1, s[18:19]
	v_lshl_add_u64 v[188:189], v[188:189], 0, s[20:21]
	s_mov_b32 m0, s13
	s_nop 0
	global_load_lds_dwordx4 v[188:189], off
	v_lshl_add_u64 v[188:189], v[158:159], 1, s[18:19]
	v_lshl_add_u64 v[188:189], v[188:189], 0, s[20:21]
	s_add_i32 m0, s13, 0x400
	s_nop 0
	global_load_lds_dwordx4 v[188:189], off

; #define LAS __attribute__((address_space(3)))
; #define VM_WAIT() asm volatile("s_waitcnt vmcnt(0)" ::: "memory")
; #define SBAR() __builtin_amdgcn_sched_barrier(0)
; template <int OFF> __device__ __forceinline__ s16x4 tr_read(int vb) { s16x4 r; asm volatile("ds_read_b64_tr_b16 %0, %1 offset:%2" : "=&v"(r) : "v"(vb), "i"(OFF) : "memory"); return r; }
; #define BAR() do { asm volatile("" ::: "memory"); __builtin_amdgcn_s_barrier(); asm volatile("" ::: "memory"); } while (0)
; __device__ __forceinline__ void qkt(f32x16& p0, f32x16& p1, const LAS char* Ks, const bf16x8 (&qr)[8], int r32, int hi) {
;     p0 = f32x16{}; p1 = f32x16{};
; #pragma unroll
;     for (int d0 = 0; d0 < 8; ++d0) { const int cb = (d0 * 16 + hi * 8) * 2;
;         const bf16x8 b0 = *(const LAS bf16x8*)(Ks + KSWZ(r32, cb));
;         const bf16x8 b1 = *(const LAS bf16x8*)(Ks + KSWZ(32 + r32, cb));
;         p0 = __builtin_amdgcn_mfma_f32_32x32x16_bf16(b0, qr[d0], p0, 0, 0, 0);
;         p1 = __builtin_amdgcn_mfma_f32_32x32x16_bf16(b1, qr[d0], p1, 0, 0, 0);
;         if (d0 == 3) SBAR(); }
; }
; template <int D0> __device__ __forceinline__ void pv_one(f32x16& od, int vb, bf16x8 pa0, bf16x8 pa1, bf16x8 pa2, bf16x8 pa3) {
;     const s16x4 l0 = tr_read<v_rd_off(D0, 0, 0)>(vb), h0 = tr_read<v_rd_off(D0, 0, 1)>(vb), l1 = tr_read<v_rd_off(D0, 1, 0)>(vb), h1 = tr_read<v_rd_off(D0, 1, 1)>(vb);
;     const s16x4 l2 = tr_read<v_rd_off(D0, 2, 0)>(vb), h2 = tr_read<v_rd_off(D0, 2, 1)>(vb), l3 = tr_read<v_rd_off(D0, 3, 0)>(vb), h3 = tr_read<v_rd_off(D0, 3, 1)>(vb);
;     asm volatile("s_waitcnt lgkmcnt(0)" ::: "memory"); SBAR();
;     ...
;     od = __builtin_amdgcn_mfma_f32_32x32x16_bf16(pa0, PK(l0, h0), od, 0, 0, 0);
;     od = __builtin_amdgcn_mfma_f32_32x32x16_bf16(pa1, PK(l1, h1), od, 0, 0, 0);
;     od = __builtin_amdgcn_mfma_f32_32x32x16_bf16(pa2, PK(l2, h2), od, 0, 0, 0);
;     od = __builtin_amdgcn_mfma_f32_32x32x16_bf16(pa3, PK(l3, h3), od, 0, 0, 0);
;     ...
; }
; template <int MODE> ...
;     ...
;         if (half == 0 && i + 1 >= 3 && i + 1 < n) DMA(i + 1, nslot);
;         if (i > 0) PV(pslot);
;         f32x16 p0, p1;
;         qkt(p0, p1, K_lds + buf * SHM, qr, r32, hi);
;         if (half == 1) VM_WAIT();
;         BAR();
;         if (half == 1 && i + 2 >= 3 && i + 2 < n) DMA(i + 2, pslot);
.LBB0_833:
	s_setprio 0
	v_sub_co_u32_e64 v2, s[14:15], s13, 1
	s_and_b64 s[14:15], s[14:15], exec
	v_readfirstlane_b32 s14, v2
	s_cselect_b32 s14, 2, s14
	s_lshl_b32 s14, s14, 14
	v_add_u32_e32 v2, s14, v165
	ds_read_b64_tr_b16 v[84:85], v2 offset:0
	ds_read_b64_tr_b16 v[86:87], v2 offset:0x800
	ds_read_b64_tr_b16 v[88:89], v2 offset:0x1000
	ds_read_b64_tr_b16 v[90:91], v2 offset:0x1800
	ds_read_b64_tr_b16 v[92:93], v2 offset:0x2000
	ds_read_b64_tr_b16 v[94:95], v2 offset:0x2800
	ds_read_b64_tr_b16 v[96:97], v2 offset:0x3000
	ds_read_b64_tr_b16 v[98:99], v2 offset:0x3800
	s_waitcnt lgkmcnt(0)
	s_nop 0
	v_mfma_f32_32x32x16_bf16 v[20:35], v[72:75], v[84:87], v[20:35]
	ds_read_b64_tr_b16 v[84:85], v2 offset:0x200
	ds_read_b64_tr_b16 v[86:87], v2 offset:0xa00
	v_lshl_add_u32 v246, s13, 14, v170
	v_add_u32_e32 v247, v246, v171
	ds_read_b128 v[212:215], v247 offset:49152
	v_mfma_f32_32x32x16_bf16 v[20:35], v[76:79], v[88:91], v[20:35]
	ds_read_b64_tr_b16 v[88:89], v2 offset:0x1200
	ds_read_b64_tr_b16 v[90:91], v2 offset:0x1a00
	ds_read_b128 v[216:219], v247 offset:57344
	v_mfma_f32_32x32x16_bf16 v[20:35], v[80:83], v[92:95], v[20:35]
	ds_read_b64_tr_b16 v[92:93], v2 offset:0x2200
	ds_read_b64_tr_b16 v[94:95], v2 offset:0x2a00
	v_add_u32_e32 v247, v246, v172
	ds_read_b128 v[220:223], v247 offset:49152
	v_mfma_f32_32x32x16_bf16 v[20:35], v[68:71], v[96:99], v[20:35]
	ds_read_b64_tr_b16 v[96:97], v2 offset:0x3200
	ds_read_b64_tr_b16 v[98:99], v2 offset:0x3a00
	ds_read_b128 v[224:227], v247 offset:57344
	s_waitcnt lgkmcnt(0)
	v_mfma_f32_32x32x16_bf16 v[36:51], v[72:75], v[84:87], v[36:51]
	ds_read_b64_tr_b16 v[84:85], v2 offset:0x400
	ds_read_b64_tr_b16 v[86:87], v2 offset:0xc00
	v_add_u32_e32 v247, v246, v173
	ds_read_b128 v[228:231], v247 offset:49152
	v_mfma_f32_32x32x16_bf16 v[36:51], v[76:79], v[88:91], v[36:51]
	ds_read_b64_tr_b16 v[88:89], v2 offset:0x1400
	ds_read_b64_tr_b16 v[90:91], v2 offset:0x1c00
	ds_read_b128 v[232:235], v247 offset:57344
	v_mfma_f32_32x32x16_bf16 v[36:51], v[80:83], v[92:95], v[36:51]
	ds_read_b64_tr_b16 v[92:93], v2 offset:0x2400
	ds_read_b64_tr_b16 v[94:95], v2 offset:0x2c00
	v_add_u32_e32 v247, v246, v174
	ds_read_b128 v[236:239], v247 offset:49152
	v_mfma_f32_32x32x16_bf16 v[36:51], v[68:71], v[96:99], v[36:51]
	ds_read_b64_tr_b16 v[96:97], v2 offset:0x3400
	ds_read_b64_tr_b16 v[98:99], v2 offset:0x3c00
	ds_read_b128 v[240:243], v247 offset:57344
	s_waitcnt lgkmcnt(0)
	v_mfma_f32_32x32x16_bf16 v[52:67], v[72:75], v[84:87], v[52:67]
	ds_read_b64_tr_b16 v[84:85], v2 offset:0x600
	ds_read_b64_tr_b16 v[86:87], v2 offset:0xe00
	v_mfma_f32_32x32x16_bf16 v[52:67], v[76:79], v[88:91], v[52:67]
	ds_read_b64_tr_b16 v[88:89], v2 offset:0x1600
	ds_read_b64_tr_b16 v[90:91], v2 offset:0x1e00
	v_mfma_f32_32x32x16_bf16 v[52:67], v[80:83], v[92:95], v[52:67]
	ds_read_b64_tr_b16 v[92:93], v2 offset:0x2600
	ds_read_b64_tr_b16 v[94:95], v2 offset:0x2e00
	v_mfma_f32_32x32x16_bf16 v[52:67], v[68:71], v[96:99], v[52:67]
	ds_read_b64_tr_b16 v[96:97], v2 offset:0x3600
	ds_read_b64_tr_b16 v[98:99], v2 offset:0x3e00
	s_waitcnt lgkmcnt(0)
	v_mfma_f32_32x32x16_bf16 v[4:19], v[72:75], v[84:87], v[4:19]
	v_mfma_f32_32x32x16_bf16 v[4:19], v[76:79], v[88:91], v[4:19]
	v_mfma_f32_32x32x16_bf16 v[4:19], v[80:83], v[92:95], v[4:19]
	v_mfma_f32_32x32x16_bf16 v[4:19], v[68:71], v[96:99], v[4:19]
	s_and_b64 vcc, exec, s[10:11]
	v_mfma_f32_32x32x16_bf16 v[68:83], v[212:215], v[124:127], 0
	v_add_u32_e32 v247, v246, v175
	ds_read_b128 v[212:215], v247 offset:49152
	v_mfma_f32_32x32x16_bf16 v[84:99], v[216:219], v[124:127], 0
	ds_read_b128 v[216:219], v247 offset:57344
	v_mfma_f32_32x32x16_bf16 v[68:83], v[220:223], v[100:103], v[68:83]
	v_add_u32_e32 v247, v246, v176
	ds_read_b128 v[220:223], v247 offset:49152
	v_mfma_f32_32x32x16_bf16 v[84:99], v[224:227], v[100:103], v[84:99]
	ds_read_b128 v[224:227], v247 offset:57344
	v_mfma_f32_32x32x16_bf16 v[68:83], v[228:231], v[104:107], v[68:83]
	v_add_u32_e32 v247, v246, v177
	ds_read_b128 v[228:231], v247 offset:49152
	v_mfma_f32_32x32x16_bf16 v[84:99], v[232:235], v[104:107], v[84:99]
	ds_read_b128 v[232:235], v247 offset:57344
	v_mfma_f32_32x32x16_bf16 v[68:83], v[236:239], v[108:111], v[68:83]
	v_add_u32_e32 v247, v246, v178
	ds_read_b128 v[236:239], v247 offset:49152
	v_mfma_f32_32x32x16_bf16 v[84:99], v[240:243], v[108:111], v[84:99]
	ds_read_b128 v[240:243], v247 offset:57344
	s_waitcnt lgkmcnt(7)
	v_mfma_f32_32x32x16_bf16 v[68:83], v[212:215], v[112:115], v[68:83]
	s_waitcnt lgkmcnt(6)
	v_mfma_f32_32x32x16_bf16 v[84:99], v[216:219], v[112:115], v[84:99]
	s_waitcnt lgkmcnt(5)
	v_mfma_f32_32x32x16_bf16 v[68:83], v[220:223], v[116:119], v[68:83]
	s_waitcnt lgkmcnt(4)
	v_mfma_f32_32x32x16_bf16 v[84:99], v[224:227], v[116:119], v[84:99]
	s_waitcnt lgkmcnt(3)
	v_mfma_f32_32x32x16_bf16 v[68:83], v[228:231], v[120:123], v[68:83]
	s_waitcnt lgkmcnt(2)
	v_mfma_f32_32x32x16_bf16 v[84:99], v[232:235], v[120:123], v[84:99]
	s_waitcnt lgkmcnt(1)
	v_mfma_f32_32x32x16_bf16 v[68:83], v[236:239], v[128:131], v[68:83]
	s_waitcnt lgkmcnt(0)
	v_mfma_f32_32x32x16_bf16 v[84:99], v[240:243], v[128:131], v[84:99]
	s_cbranch_vccnz .LBB0_835
	s_waitcnt vmcnt(0)
.LBB0_835:
	s_setprio 1
	s_barrier
	s_and_b64 vcc, exec, s[10:11]
	s_cbranch_vccnz .LBB0_838
	s_add_i32 s13, s72, 2
	s_cmp_ge_i32 s13, s31
	s_cbranch_scc1 .LBB0_838
	v_mov_b32_e32 v2, s97
	ds_read_b32 v2, v2
	s_waitcnt lgkmcnt(0)
	v_readfirstlane_b32 s13, v2
	s_mul_hi_i32 s15, s13, 0x1e8000
	s_mul_i32 s13, s13, 0x1e8000
	s_add_u32 s16, s94, s13
	s_addc_u32 s17, s2, s15
	s_add_i32 s18, s90, s14
	s_add_i32 m0, s18, 0xc000
	v_lshl_add_u64 v[186:187], v[152:153], 1, s[16:17]
	global_load_lds_dwordx4 v[186:187], off
	s_add_i32 m0, s18, 0xc400
	s_add_u32 s14, s3, s13
	v_lshl_add_u64 v[186:187], v[156:157], 1, s[16:17]
	s_addc_u32 s15, s6, s15
	global_load_lds_dwordx4 v[186:187], off
	v_lshl_add_u64 v[186:187], v[154:155], 1, s[14:15]
	s_mov_b32 m0, s18
	s_nop 0
	global_load_lds_dwordx4 v[186:187], off
	v_lshl_add_u64 v[186:187], v[158:159], 1, s[14:15]
	s_add_i32 m0, s18, 0x400
	s_nop 0
	global_load_lds_dwordx4 v[186:187], off
